# merge epilogue: the once-read gate tile g0 of the first branch unit loaded with the nt hint
# baseline (speedup 1.0000x reference)
.LBB0_1217:
	s_ashr_i32 s30, s63, 2
	s_lshl_b32 s4, s30, 15
	s_lshl_b32 s5, s67, 8
	s_sub_i32 s4, s5, s4
	v_add_u32_e32 v2, s4, v165
	s_lshl_b32 s5, s63, 8
	s_and_b32 s5, s5, 0x300
	v_add_u32_e32 v0, s5, v189
	v_mul_u32_u24_e32 v191, 0x1800, v2
	v_lshl_add_u32 v191, v0, 1, v191
	v_lshlrev_b32_e32 v3, 11, v2
	v_lshl_add_u32 v3, v0, 1, v3
	v_bfe_u32 v2, v165, 6, 1
	v_lshlrev_b32_e32 v2, 12, v2
	v_bfe_u32 v0, v189, 5, 2
	v_lshl_add_u32 v2, v0, 10, v2
	v_bfe_u32 v0, v189, 3, 2
	v_lshl_add_u32 v2, v0, 8, v2
	v_and_b32_e32 v0, 15, v165
	v_lshl_add_u32 v2, v0, 4, v2
	v_add_u32_e32 v2, 0x21000, v2
	s_lshl_b32 s26, s30, 11
	s_add_u32 s26, s14, s26
	s_addc_u32 s27, s15, 0
	s_cmp_eq_u32 s30, 2
	s_cbranch_scc1 .Lmg_last
	s_cmp_eq_u32 s30, 1
	s_cbranch_scc1 .Lmg_mid
	s_add_u32 s28, s26, 0x0
	s_addc_u32 s29, s27, 0
	global_load_dwordx4 v[132:135], v191, s[28:29] nt
	global_load_dwordx4 v[136:139], v191, s[28:29] offset:2048
	s_add_u32 s28, s26, 0x0
	s_addc_u32 s29, s27, 0
	global_load_dwordx4 v[140:143], v191, s[28:29] offset:256 nt
	global_load_dwordx4 v[144:147], v191, s[28:29] offset:2304
	s_add_u32 s28, s26, 0x18000
	s_addc_u32 s29, s27, 0
	global_load_dwordx4 v[148:151], v191, s[28:29] nt
	global_load_dwordx4 v[152:155], v191, s[28:29] offset:2048
	s_add_u32 s28, s26, 0x18000
	s_addc_u32 s29, s27, 0
	global_load_dwordx4 v[156:159], v191, s[28:29] offset:256 nt
	global_load_dwordx4 v[160:163], v191, s[28:29] offset:2304
	s_add_u32 s28, s26, 0x30000
	s_addc_u32 s29, s27, 0
	global_load_dwordx4 v[180:183], v191, s[28:29] nt
	global_load_dwordx4 v[184:187], v191, s[28:29] offset:2048
	s_add_u32 s28, s26, 0x30000
	s_addc_u32 s29, s27, 0
	global_load_dwordx4 v[192:195], v191, s[28:29] offset:256 nt
	global_load_dwordx4 v[196:199], v191, s[28:29] offset:2304
	s_add_u32 s28, s26, 0x48000
	s_addc_u32 s29, s27, 0
	global_load_dwordx4 v[212:215], v191, s[28:29] nt
	global_load_dwordx4 v[216:219], v191, s[28:29] offset:2048
	s_and_b64 vcc, exec, s[20:21]
	s_cbranch_vccz .Lmg_nba
	s_barrier
.Lmg_nba:
	s_waitcnt vmcnt(12)
	v_lshlrev_b32_e32 v220, 16, v132
	v_and_b32_e32 v221, 0xffff0000, v132
	v_lshlrev_b32_e32 v222, 16, v133
	v_and_b32_e32 v223, 0xffff0000, v133
	v_lshlrev_b32_e32 v224, 16, v134
	v_and_b32_e32 v225, 0xffff0000, v134
	v_lshlrev_b32_e32 v226, 16, v135
	v_and_b32_e32 v227, 0xffff0000, v135
	v_max_f32_e32 v220, 0x1e3ce508, v220
	v_max_f32_e32 v221, 0x1e3ce508, v221
	v_max_f32_e32 v222, 0x1e3ce508, v222
	v_max_f32_e32 v223, 0x1e3ce508, v223
	v_max_f32_e32 v224, 0x1e3ce508, v224
	v_max_f32_e32 v225, 0x1e3ce508, v225
	v_max_f32_e32 v226, 0x1e3ce508, v226
	v_max_f32_e32 v227, 0x1e3ce508, v227
	v_mov_b32_e32 v228, v136
	v_mov_b32_e32 v229, v137
	v_mov_b32_e32 v230, v138
	v_mov_b32_e32 v231, v139
	v_lshlrev_b32_e32 v132, 16, v136
	v_and_b32_e32 v133, 0xffff0000, v136
	v_lshlrev_b32_e32 v134, 16, v137
	v_and_b32_e32 v135, 0xffff0000, v137
	v_lshlrev_b32_e32 v136, 16, v138
	v_and_b32_e32 v137, 0xffff0000, v138
	v_lshlrev_b32_e32 v138, 16, v139
	v_and_b32_e32 v139, 0xffff0000, v139
	v_max_f32_e32 v132, 0x1e3ce508, v132
	v_max_f32_e32 v133, 0x1e3ce508, v133
	v_max_f32_e32 v134, 0x1e3ce508, v134
	v_max_f32_e32 v135, 0x1e3ce508, v135
	v_max_f32_e32 v136, 0x1e3ce508, v136
	v_max_f32_e32 v137, 0x1e3ce508, v137
	v_max_f32_e32 v138, 0x1e3ce508, v138
	v_max_f32_e32 v139, 0x1e3ce508, v139
	v_rcp_f32_e32 v132, v132
	v_rcp_f32_e32 v133, v133
	v_rcp_f32_e32 v134, v134
	v_rcp_f32_e32 v135, v135
	v_rcp_f32_e32 v136, v136
	v_rcp_f32_e32 v137, v137
	v_rcp_f32_e32 v138, v138
	v_rcp_f32_e32 v139, v139
	v_pk_mul_f32 v[220:221], v[220:221], v[132:133]
	v_pk_mul_f32 v[222:223], v[222:223], v[134:135]
	v_pk_mul_f32 v[224:225], v[224:225], v[136:137]
	v_pk_mul_f32 v[226:227], v[226:227], v[138:139]
	v_pk_mul_f32 v[112:113], v[112:113], v[220:221]
	v_pk_mul_f32 v[114:115], v[114:115], v[222:223]
	v_pk_mul_f32 v[108:109], v[108:109], v[224:225]
	v_pk_mul_f32 v[110:111], v[110:111], v[226:227]
	s_add_u32 s28, s26, 0x48000
	s_addc_u32 s29, s27, 0
	global_load_dwordx4 v[132:135], v191, s[28:29] offset:256 nt
	global_load_dwordx4 v[136:139], v191, s[28:29] offset:2304
	s_waitcnt vmcnt(12)
	v_lshlrev_b32_e32 v220, 16, v140
	v_and_b32_e32 v221, 0xffff0000, v140
	v_lshlrev_b32_e32 v222, 16, v141
	v_and_b32_e32 v223, 0xffff0000, v141
	v_lshlrev_b32_e32 v224, 16, v142
	v_and_b32_e32 v225, 0xffff0000, v142
	v_lshlrev_b32_e32 v226, 16, v143
	v_and_b32_e32 v227, 0xffff0000, v143
	v_max_f32_e32 v220, 0x1e3ce508, v220
	v_max_f32_e32 v221, 0x1e3ce508, v221
	v_max_f32_e32 v222, 0x1e3ce508, v222
	v_max_f32_e32 v223, 0x1e3ce508, v223
	v_max_f32_e32 v224, 0x1e3ce508, v224
	v_max_f32_e32 v225, 0x1e3ce508, v225
	v_max_f32_e32 v226, 0x1e3ce508, v226
	v_max_f32_e32 v227, 0x1e3ce508, v227
	v_mov_b32_e32 v232, v144
	v_mov_b32_e32 v233, v145
	v_mov_b32_e32 v234, v146
	v_mov_b32_e32 v235, v147
	v_lshlrev_b32_e32 v140, 16, v144
	v_and_b32_e32 v141, 0xffff0000, v144
	v_lshlrev_b32_e32 v142, 16, v145
	v_and_b32_e32 v143, 0xffff0000, v145
	v_lshlrev_b32_e32 v144, 16, v146
	v_and_b32_e32 v145, 0xffff0000, v146
	v_lshlrev_b32_e32 v146, 16, v147
	v_and_b32_e32 v147, 0xffff0000, v147
	v_max_f32_e32 v140, 0x1e3ce508, v140
	v_max_f32_e32 v141, 0x1e3ce508, v141
	v_max_f32_e32 v142, 0x1e3ce508, v142
	v_max_f32_e32 v143, 0x1e3ce508, v143
	v_max_f32_e32 v144, 0x1e3ce508, v144
	v_max_f32_e32 v145, 0x1e3ce508, v145
	v_max_f32_e32 v146, 0x1e3ce508, v146
	v_max_f32_e32 v147, 0x1e3ce508, v147
	v_rcp_f32_e32 v140, v140
	v_rcp_f32_e32 v141, v141
	v_rcp_f32_e32 v142, v142
	v_rcp_f32_e32 v143, v143
	v_rcp_f32_e32 v144, v144
	v_rcp_f32_e32 v145, v145
	v_rcp_f32_e32 v146, v146
	v_rcp_f32_e32 v147, v147
	v_pk_mul_f32 v[220:221], v[220:221], v[140:141]
	v_pk_mul_f32 v[222:223], v[222:223], v[142:143]
	v_pk_mul_f32 v[224:225], v[224:225], v[144:145]
	v_pk_mul_f32 v[226:227], v[226:227], v[146:147]
	v_pk_mul_f32 v[80:81], v[80:81], v[220:221]
	v_pk_mul_f32 v[82:83], v[82:83], v[222:223]
	v_pk_mul_f32 v[76:77], v[76:77], v[224:225]
	v_pk_mul_f32 v[78:79], v[78:79], v[226:227]
	s_add_u32 s28, s26, 0xc0000
	s_addc_u32 s29, s27, 0
	global_load_dwordx4 v[140:143], v191, s[28:29] nt
	global_load_dwordx4 v[144:147], v191, s[28:29] offset:2048
	s_waitcnt vmcnt(12)
	v_lshlrev_b32_e32 v220, 16, v148
	v_and_b32_e32 v221, 0xffff0000, v148
	v_lshlrev_b32_e32 v222, 16, v149
	v_and_b32_e32 v223, 0xffff0000, v149
	v_lshlrev_b32_e32 v224, 16, v150
	v_and_b32_e32 v225, 0xffff0000, v150
	v_lshlrev_b32_e32 v226, 16, v151
	v_and_b32_e32 v227, 0xffff0000, v151
	v_max_f32_e32 v220, 0x1e3ce508, v220
	v_max_f32_e32 v221, 0x1e3ce508, v221
	v_max_f32_e32 v222, 0x1e3ce508, v222
	v_max_f32_e32 v223, 0x1e3ce508, v223
	v_max_f32_e32 v224, 0x1e3ce508, v224
	v_max_f32_e32 v225, 0x1e3ce508, v225
	v_max_f32_e32 v226, 0x1e3ce508, v226
	v_max_f32_e32 v227, 0x1e3ce508, v227
	v_mov_b32_e32 v236, v152
	v_mov_b32_e32 v237, v153
	v_mov_b32_e32 v238, v154
	v_mov_b32_e32 v239, v155
	v_lshlrev_b32_e32 v148, 16, v152
	v_and_b32_e32 v149, 0xffff0000, v152
	v_lshlrev_b32_e32 v150, 16, v153
	v_and_b32_e32 v151, 0xffff0000, v153
	v_lshlrev_b32_e32 v152, 16, v154
	v_and_b32_e32 v153, 0xffff0000, v154
	v_lshlrev_b32_e32 v154, 16, v155
	v_and_b32_e32 v155, 0xffff0000, v155
	v_max_f32_e32 v148, 0x1e3ce508, v148
	v_max_f32_e32 v149, 0x1e3ce508, v149
	v_max_f32_e32 v150, 0x1e3ce508, v150
	v_max_f32_e32 v151, 0x1e3ce508, v151
	v_max_f32_e32 v152, 0x1e3ce508, v152
	v_max_f32_e32 v153, 0x1e3ce508, v153
	v_max_f32_e32 v154, 0x1e3ce508, v154
	v_max_f32_e32 v155, 0x1e3ce508, v155
	v_rcp_f32_e32 v148, v148
	v_rcp_f32_e32 v149, v149
	v_rcp_f32_e32 v150, v150
	v_rcp_f32_e32 v151, v151
	v_rcp_f32_e32 v152, v152
	v_rcp_f32_e32 v153, v153
	v_rcp_f32_e32 v154, v154
	v_rcp_f32_e32 v155, v155
	v_pk_mul_f32 v[220:221], v[220:221], v[148:149]
	v_pk_mul_f32 v[222:223], v[222:223], v[150:151]
	v_pk_mul_f32 v[224:225], v[224:225], v[152:153]
	v_pk_mul_f32 v[226:227], v[226:227], v[154:155]
	v_pk_mul_f32 v[104:105], v[104:105], v[220:221]
	v_pk_mul_f32 v[106:107], v[106:107], v[222:223]
	v_pk_mul_f32 v[100:101], v[100:101], v[224:225]
	v_pk_mul_f32 v[102:103], v[102:103], v[226:227]
	s_add_u32 s28, s26, 0xc0000
	s_addc_u32 s29, s27, 0
	global_load_dwordx4 v[148:151], v191, s[28:29] offset:256 nt
	global_load_dwordx4 v[152:155], v191, s[28:29] offset:2304
	s_waitcnt vmcnt(12)
	v_lshlrev_b32_e32 v220, 16, v156
	v_and_b32_e32 v221, 0xffff0000, v156
	v_lshlrev_b32_e32 v222, 16, v157
	v_and_b32_e32 v223, 0xffff0000, v157
	v_lshlrev_b32_e32 v224, 16, v158
	v_and_b32_e32 v225, 0xffff0000, v158
	v_lshlrev_b32_e32 v226, 16, v159
	v_and_b32_e32 v227, 0xffff0000, v159
	v_max_f32_e32 v220, 0x1e3ce508, v220
	v_max_f32_e32 v221, 0x1e3ce508, v221
	v_max_f32_e32 v222, 0x1e3ce508, v222
	v_max_f32_e32 v223, 0x1e3ce508, v223
	v_max_f32_e32 v224, 0x1e3ce508, v224
	v_max_f32_e32 v225, 0x1e3ce508, v225
	v_max_f32_e32 v226, 0x1e3ce508, v226
	v_max_f32_e32 v227, 0x1e3ce508, v227
	v_mov_b32_e32 v240, v160
	v_mov_b32_e32 v241, v161
	v_mov_b32_e32 v242, v162
	v_mov_b32_e32 v243, v163
	v_lshlrev_b32_e32 v156, 16, v160
	v_and_b32_e32 v157, 0xffff0000, v160
	v_lshlrev_b32_e32 v158, 16, v161
	v_and_b32_e32 v159, 0xffff0000, v161
	v_lshlrev_b32_e32 v160, 16, v162
	v_and_b32_e32 v161, 0xffff0000, v162
	v_lshlrev_b32_e32 v162, 16, v163
	v_and_b32_e32 v163, 0xffff0000, v163
	v_max_f32_e32 v156, 0x1e3ce508, v156
	v_max_f32_e32 v157, 0x1e3ce508, v157
	v_max_f32_e32 v158, 0x1e3ce508, v158
	v_max_f32_e32 v159, 0x1e3ce508, v159
	v_max_f32_e32 v160, 0x1e3ce508, v160
	v_max_f32_e32 v161, 0x1e3ce508, v161
	v_max_f32_e32 v162, 0x1e3ce508, v162
	v_max_f32_e32 v163, 0x1e3ce508, v163
	v_rcp_f32_e32 v156, v156
	v_rcp_f32_e32 v157, v157
	v_rcp_f32_e32 v158, v158
	v_rcp_f32_e32 v159, v159
	v_rcp_f32_e32 v160, v160
	v_rcp_f32_e32 v161, v161
	v_rcp_f32_e32 v162, v162
	v_rcp_f32_e32 v163, v163
	v_pk_mul_f32 v[220:221], v[220:221], v[156:157]
	v_pk_mul_f32 v[222:223], v[222:223], v[158:159]
	v_pk_mul_f32 v[224:225], v[224:225], v[160:161]
	v_pk_mul_f32 v[226:227], v[226:227], v[162:163]
	v_pk_mul_f32 v[72:73], v[72:73], v[220:221]
	v_pk_mul_f32 v[74:75], v[74:75], v[222:223]
	v_pk_mul_f32 v[68:69], v[68:69], v[224:225]
	v_pk_mul_f32 v[70:71], v[70:71], v[226:227]
	s_add_u32 s28, s26, 0xd8000
	s_addc_u32 s29, s27, 0
	global_load_dwordx4 v[156:159], v191, s[28:29] nt
	global_load_dwordx4 v[160:163], v191, s[28:29] offset:2048
	s_waitcnt vmcnt(12)
	v_lshlrev_b32_e32 v220, 16, v180
	v_and_b32_e32 v221, 0xffff0000, v180
	v_lshlrev_b32_e32 v222, 16, v181
	v_and_b32_e32 v223, 0xffff0000, v181
	v_lshlrev_b32_e32 v224, 16, v182
	v_and_b32_e32 v225, 0xffff0000, v182
	v_lshlrev_b32_e32 v226, 16, v183
	v_and_b32_e32 v227, 0xffff0000, v183
	v_max_f32_e32 v220, 0x1e3ce508, v220
	v_max_f32_e32 v221, 0x1e3ce508, v221
	v_max_f32_e32 v222, 0x1e3ce508, v222
	v_max_f32_e32 v223, 0x1e3ce508, v223
	v_max_f32_e32 v224, 0x1e3ce508, v224
	v_max_f32_e32 v225, 0x1e3ce508, v225
	v_max_f32_e32 v226, 0x1e3ce508, v226
	v_max_f32_e32 v227, 0x1e3ce508, v227
	v_mov_b32_e32 v244, v184
	v_mov_b32_e32 v245, v185
	v_mov_b32_e32 v246, v186
	v_mov_b32_e32 v247, v187
	v_lshlrev_b32_e32 v180, 16, v184
	v_and_b32_e32 v181, 0xffff0000, v184
	v_lshlrev_b32_e32 v182, 16, v185
	v_and_b32_e32 v183, 0xffff0000, v185
	v_lshlrev_b32_e32 v184, 16, v186
	v_and_b32_e32 v185, 0xffff0000, v186
	v_lshlrev_b32_e32 v186, 16, v187
	v_and_b32_e32 v187, 0xffff0000, v187
	v_max_f32_e32 v180, 0x1e3ce508, v180
	v_max_f32_e32 v181, 0x1e3ce508, v181
	v_max_f32_e32 v182, 0x1e3ce508, v182
	v_max_f32_e32 v183, 0x1e3ce508, v183
	v_max_f32_e32 v184, 0x1e3ce508, v184
	v_max_f32_e32 v185, 0x1e3ce508, v185
	v_max_f32_e32 v186, 0x1e3ce508, v186
	v_max_f32_e32 v187, 0x1e3ce508, v187
	v_rcp_f32_e32 v180, v180
	v_rcp_f32_e32 v181, v181
	v_rcp_f32_e32 v182, v182
	v_rcp_f32_e32 v183, v183
	v_rcp_f32_e32 v184, v184
	v_rcp_f32_e32 v185, v185
	v_rcp_f32_e32 v186, v186
	v_rcp_f32_e32 v187, v187
	v_pk_mul_f32 v[220:221], v[220:221], v[180:181]
	v_pk_mul_f32 v[222:223], v[222:223], v[182:183]
	v_pk_mul_f32 v[224:225], v[224:225], v[184:185]
	v_pk_mul_f32 v[226:227], v[226:227], v[186:187]
	v_pk_mul_f32 v[96:97], v[96:97], v[220:221]
	v_pk_mul_f32 v[98:99], v[98:99], v[222:223]
	v_pk_mul_f32 v[92:93], v[92:93], v[224:225]
	v_pk_mul_f32 v[94:95], v[94:95], v[226:227]
	s_add_u32 s28, s26, 0xd8000
	s_addc_u32 s29, s27, 0
	global_load_dwordx4 v[180:183], v191, s[28:29] offset:256 nt
	global_load_dwordx4 v[184:187], v191, s[28:29] offset:2304
	s_waitcnt vmcnt(12)
	v_lshlrev_b32_e32 v220, 16, v192
	v_and_b32_e32 v221, 0xffff0000, v192
	v_lshlrev_b32_e32 v222, 16, v193
	v_and_b32_e32 v223, 0xffff0000, v193
	v_lshlrev_b32_e32 v224, 16, v194
	v_and_b32_e32 v225, 0xffff0000, v194
	v_lshlrev_b32_e32 v226, 16, v195
	v_and_b32_e32 v227, 0xffff0000, v195
	v_max_f32_e32 v220, 0x1e3ce508, v220
	v_max_f32_e32 v221, 0x1e3ce508, v221
	v_max_f32_e32 v222, 0x1e3ce508, v222
	v_max_f32_e32 v223, 0x1e3ce508, v223
	v_max_f32_e32 v224, 0x1e3ce508, v224
	v_max_f32_e32 v225, 0x1e3ce508, v225
	v_max_f32_e32 v226, 0x1e3ce508, v226
	v_max_f32_e32 v227, 0x1e3ce508, v227
	v_mov_b32_e32 v248, v196
	v_mov_b32_e32 v249, v197
	v_mov_b32_e32 v250, v198
	v_mov_b32_e32 v251, v199
	v_lshlrev_b32_e32 v192, 16, v196
	v_and_b32_e32 v193, 0xffff0000, v196
	v_lshlrev_b32_e32 v194, 16, v197
	v_and_b32_e32 v195, 0xffff0000, v197
	v_lshlrev_b32_e32 v196, 16, v198
	v_and_b32_e32 v197, 0xffff0000, v198
	v_lshlrev_b32_e32 v198, 16, v199
	v_and_b32_e32 v199, 0xffff0000, v199
	v_max_f32_e32 v192, 0x1e3ce508, v192
	v_max_f32_e32 v193, 0x1e3ce508, v193
	v_max_f32_e32 v194, 0x1e3ce508, v194
	v_max_f32_e32 v195, 0x1e3ce508, v195
	v_max_f32_e32 v196, 0x1e3ce508, v196
	v_max_f32_e32 v197, 0x1e3ce508, v197
	v_max_f32_e32 v198, 0x1e3ce508, v198
	v_max_f32_e32 v199, 0x1e3ce508, v199
	v_rcp_f32_e32 v192, v192
	v_rcp_f32_e32 v193, v193
	v_rcp_f32_e32 v194, v194
	v_rcp_f32_e32 v195, v195
	v_rcp_f32_e32 v196, v196
	v_rcp_f32_e32 v197, v197
	v_rcp_f32_e32 v198, v198
	v_rcp_f32_e32 v199, v199
	v_pk_mul_f32 v[220:221], v[220:221], v[192:193]
	v_pk_mul_f32 v[222:223], v[222:223], v[194:195]
	v_pk_mul_f32 v[224:225], v[224:225], v[196:197]
	v_pk_mul_f32 v[226:227], v[226:227], v[198:199]
	v_pk_mul_f32 v[64:65], v[64:65], v[220:221]
	v_pk_mul_f32 v[66:67], v[66:67], v[222:223]
	v_pk_mul_f32 v[60:61], v[60:61], v[224:225]
	v_pk_mul_f32 v[62:63], v[62:63], v[226:227]
	s_add_u32 s28, s26, 0xf0000
	s_addc_u32 s29, s27, 0
	global_load_dwordx4 v[192:195], v191, s[28:29] nt
	global_load_dwordx4 v[196:199], v191, s[28:29] offset:2048
	s_waitcnt vmcnt(12)
	v_lshlrev_b32_e32 v220, 16, v212
	v_and_b32_e32 v221, 0xffff0000, v212
	v_lshlrev_b32_e32 v222, 16, v213
	v_and_b32_e32 v223, 0xffff0000, v213
	v_lshlrev_b32_e32 v224, 16, v214
	v_and_b32_e32 v225, 0xffff0000, v214
	v_lshlrev_b32_e32 v226, 16, v215
	v_and_b32_e32 v227, 0xffff0000, v215
	v_max_f32_e32 v220, 0x1e3ce508, v220
	v_max_f32_e32 v221, 0x1e3ce508, v221
	v_max_f32_e32 v222, 0x1e3ce508, v222
	v_max_f32_e32 v223, 0x1e3ce508, v223
	v_max_f32_e32 v224, 0x1e3ce508, v224
	v_max_f32_e32 v225, 0x1e3ce508, v225
	v_max_f32_e32 v226, 0x1e3ce508, v226
	v_max_f32_e32 v227, 0x1e3ce508, v227
	v_mov_b32_e32 v168, v216
	v_mov_b32_e32 v169, v217
	v_mov_b32_e32 v170, v218
	v_mov_b32_e32 v171, v219
	v_lshlrev_b32_e32 v212, 16, v216
	v_and_b32_e32 v213, 0xffff0000, v216
	v_lshlrev_b32_e32 v214, 16, v217
	v_and_b32_e32 v215, 0xffff0000, v217
	v_lshlrev_b32_e32 v216, 16, v218
	v_and_b32_e32 v217, 0xffff0000, v218
	v_lshlrev_b32_e32 v218, 16, v219
	v_and_b32_e32 v219, 0xffff0000, v219
	v_max_f32_e32 v212, 0x1e3ce508, v212
	v_max_f32_e32 v213, 0x1e3ce508, v213
	v_max_f32_e32 v214, 0x1e3ce508, v214
	v_max_f32_e32 v215, 0x1e3ce508, v215
	v_max_f32_e32 v216, 0x1e3ce508, v216
	v_max_f32_e32 v217, 0x1e3ce508, v217
	v_max_f32_e32 v218, 0x1e3ce508, v218
	v_max_f32_e32 v219, 0x1e3ce508, v219
	v_rcp_f32_e32 v212, v212
	v_rcp_f32_e32 v213, v213
	v_rcp_f32_e32 v214, v214
	v_rcp_f32_e32 v215, v215
	v_rcp_f32_e32 v216, v216
	v_rcp_f32_e32 v217, v217
	v_rcp_f32_e32 v218, v218
	v_rcp_f32_e32 v219, v219
	v_pk_mul_f32 v[220:221], v[220:221], v[212:213]
	v_pk_mul_f32 v[222:223], v[222:223], v[214:215]
	v_pk_mul_f32 v[224:225], v[224:225], v[216:217]
	v_pk_mul_f32 v[226:227], v[226:227], v[218:219]
	v_pk_mul_f32 v[88:89], v[88:89], v[220:221]
	v_pk_mul_f32 v[90:91], v[90:91], v[222:223]
	v_pk_mul_f32 v[84:85], v[84:85], v[224:225]
	v_pk_mul_f32 v[86:87], v[86:87], v[226:227]
	s_add_u32 s28, s26, 0xf0000
	s_addc_u32 s29, s27, 0
	global_load_dwordx4 v[212:215], v191, s[28:29] offset:256 nt
	global_load_dwordx4 v[216:219], v191, s[28:29] offset:2304
	s_waitcnt vmcnt(12)
	v_lshlrev_b32_e32 v220, 16, v132
	v_and_b32_e32 v221, 0xffff0000, v132
	v_lshlrev_b32_e32 v222, 16, v133
	v_and_b32_e32 v223, 0xffff0000, v133
	v_lshlrev_b32_e32 v224, 16, v134
	v_and_b32_e32 v225, 0xffff0000, v134
	v_lshlrev_b32_e32 v226, 16, v135
	v_and_b32_e32 v227, 0xffff0000, v135
	v_max_f32_e32 v220, 0x1e3ce508, v220
	v_max_f32_e32 v221, 0x1e3ce508, v221
	v_max_f32_e32 v222, 0x1e3ce508, v222
	v_max_f32_e32 v223, 0x1e3ce508, v223
	v_max_f32_e32 v224, 0x1e3ce508, v224
	v_max_f32_e32 v225, 0x1e3ce508, v225
	v_max_f32_e32 v226, 0x1e3ce508, v226
	v_max_f32_e32 v227, 0x1e3ce508, v227
	v_lshlrev_b32_e32 v132, 16, v136
	v_and_b32_e32 v133, 0xffff0000, v136
	v_lshlrev_b32_e32 v134, 16, v137
	v_and_b32_e32 v135, 0xffff0000, v137
	v_lshlrev_b32_e32 v136, 16, v138
	v_and_b32_e32 v137, 0xffff0000, v138
	v_lshlrev_b32_e32 v138, 16, v139
	v_and_b32_e32 v139, 0xffff0000, v139
	v_max_f32_e32 v132, 0x1e3ce508, v132
	v_max_f32_e32 v133, 0x1e3ce508, v133
	v_max_f32_e32 v134, 0x1e3ce508, v134
	v_max_f32_e32 v135, 0x1e3ce508, v135
	v_max_f32_e32 v136, 0x1e3ce508, v136
	v_max_f32_e32 v137, 0x1e3ce508, v137
	v_max_f32_e32 v138, 0x1e3ce508, v138
	v_max_f32_e32 v139, 0x1e3ce508, v139
	v_rcp_f32_e32 v132, v132
	v_rcp_f32_e32 v133, v133
	v_rcp_f32_e32 v134, v134
	v_rcp_f32_e32 v135, v135
	v_rcp_f32_e32 v136, v136
	v_rcp_f32_e32 v137, v137
	v_rcp_f32_e32 v138, v138
	v_rcp_f32_e32 v139, v139
	v_pk_mul_f32 v[220:221], v[220:221], v[132:133]
	v_pk_mul_f32 v[222:223], v[222:223], v[134:135]
	v_pk_mul_f32 v[224:225], v[224:225], v[136:137]
	v_pk_mul_f32 v[226:227], v[226:227], v[138:139]
	v_pk_mul_f32 v[56:57], v[56:57], v[220:221]
	v_pk_mul_f32 v[58:59], v[58:59], v[222:223]
	v_pk_mul_f32 v[48:49], v[48:49], v[224:225]
	v_pk_mul_f32 v[50:51], v[50:51], v[226:227]
	s_add_u32 s28, s26, 0x108000
	s_addc_u32 s29, s27, 0
	global_load_dwordx4 v[132:135], v191, s[28:29] nt
	global_load_dwordx4 v[136:139], v191, s[28:29] offset:2048
	s_waitcnt vmcnt(12)
	v_lshlrev_b32_e32 v220, 16, v140
	v_and_b32_e32 v221, 0xffff0000, v140
	v_lshlrev_b32_e32 v222, 16, v141
	v_and_b32_e32 v223, 0xffff0000, v141
	v_lshlrev_b32_e32 v224, 16, v142
	v_and_b32_e32 v225, 0xffff0000, v142
	v_lshlrev_b32_e32 v226, 16, v143
	v_and_b32_e32 v227, 0xffff0000, v143
	v_max_f32_e32 v220, 0x1e3ce508, v220
	v_max_f32_e32 v221, 0x1e3ce508, v221
	v_max_f32_e32 v222, 0x1e3ce508, v222
	v_max_f32_e32 v223, 0x1e3ce508, v223
	v_max_f32_e32 v224, 0x1e3ce508, v224
	v_max_f32_e32 v225, 0x1e3ce508, v225
	v_max_f32_e32 v226, 0x1e3ce508, v226
	v_max_f32_e32 v227, 0x1e3ce508, v227
	v_lshlrev_b32_e32 v140, 16, v144
	v_and_b32_e32 v141, 0xffff0000, v144
	v_lshlrev_b32_e32 v142, 16, v145
	v_and_b32_e32 v143, 0xffff0000, v145
	v_lshlrev_b32_e32 v144, 16, v146
	v_and_b32_e32 v145, 0xffff0000, v146
	v_lshlrev_b32_e32 v146, 16, v147
	v_and_b32_e32 v147, 0xffff0000, v147
	v_max_f32_e32 v140, 0x1e3ce508, v140
	v_max_f32_e32 v141, 0x1e3ce508, v141
	v_max_f32_e32 v142, 0x1e3ce508, v142
	v_max_f32_e32 v143, 0x1e3ce508, v143
	v_max_f32_e32 v144, 0x1e3ce508, v144
	v_max_f32_e32 v145, 0x1e3ce508, v145
	v_max_f32_e32 v146, 0x1e3ce508, v146
	v_max_f32_e32 v147, 0x1e3ce508, v147
	v_rcp_f32_e32 v140, v140
	v_rcp_f32_e32 v141, v141
	v_rcp_f32_e32 v142, v142
	v_rcp_f32_e32 v143, v143
	v_rcp_f32_e32 v144, v144
	v_rcp_f32_e32 v145, v145
	v_rcp_f32_e32 v146, v146
	v_rcp_f32_e32 v147, v147
	v_pk_mul_f32 v[220:221], v[220:221], v[140:141]
	v_pk_mul_f32 v[222:223], v[222:223], v[142:143]
	v_pk_mul_f32 v[224:225], v[224:225], v[144:145]
	v_pk_mul_f32 v[226:227], v[226:227], v[146:147]
	v_pk_mul_f32 v[52:53], v[52:53], v[220:221]
	v_pk_mul_f32 v[54:55], v[54:55], v[222:223]
	v_pk_mul_f32 v[44:45], v[44:45], v[224:225]
	v_pk_mul_f32 v[46:47], v[46:47], v[226:227]
	s_add_u32 s28, s26, 0x108000
	s_addc_u32 s29, s27, 0
	global_load_dwordx4 v[140:143], v191, s[28:29] offset:256 nt
	global_load_dwordx4 v[144:147], v191, s[28:29] offset:2304
	s_waitcnt vmcnt(12)
	v_lshlrev_b32_e32 v220, 16, v148
	v_and_b32_e32 v221, 0xffff0000, v148
	v_lshlrev_b32_e32 v222, 16, v149
	v_and_b32_e32 v223, 0xffff0000, v149
	v_lshlrev_b32_e32 v224, 16, v150
	v_and_b32_e32 v225, 0xffff0000, v150
	v_lshlrev_b32_e32 v226, 16, v151
	v_and_b32_e32 v227, 0xffff0000, v151
	v_max_f32_e32 v220, 0x1e3ce508, v220
	v_max_f32_e32 v221, 0x1e3ce508, v221
	v_max_f32_e32 v222, 0x1e3ce508, v222
	v_max_f32_e32 v223, 0x1e3ce508, v223
	v_max_f32_e32 v224, 0x1e3ce508, v224
	v_max_f32_e32 v225, 0x1e3ce508, v225
	v_max_f32_e32 v226, 0x1e3ce508, v226
	v_max_f32_e32 v227, 0x1e3ce508, v227
	v_lshlrev_b32_e32 v148, 16, v152
	v_and_b32_e32 v149, 0xffff0000, v152
	v_lshlrev_b32_e32 v150, 16, v153
	v_and_b32_e32 v151, 0xffff0000, v153
	v_lshlrev_b32_e32 v152, 16, v154
	v_and_b32_e32 v153, 0xffff0000, v154
	v_lshlrev_b32_e32 v154, 16, v155
	v_and_b32_e32 v155, 0xffff0000, v155
	v_max_f32_e32 v148, 0x1e3ce508, v148
	v_max_f32_e32 v149, 0x1e3ce508, v149
	v_max_f32_e32 v150, 0x1e3ce508, v150
	v_max_f32_e32 v151, 0x1e3ce508, v151
	v_max_f32_e32 v152, 0x1e3ce508, v152
	v_max_f32_e32 v153, 0x1e3ce508, v153
	v_max_f32_e32 v154, 0x1e3ce508, v154
	v_max_f32_e32 v155, 0x1e3ce508, v155
	v_rcp_f32_e32 v148, v148
	v_rcp_f32_e32 v149, v149
	v_rcp_f32_e32 v150, v150
	v_rcp_f32_e32 v151, v151
	v_rcp_f32_e32 v152, v152
	v_rcp_f32_e32 v153, v153
	v_rcp_f32_e32 v154, v154
	v_rcp_f32_e32 v155, v155
	v_pk_mul_f32 v[220:221], v[220:221], v[148:149]
	v_pk_mul_f32 v[222:223], v[222:223], v[150:151]
	v_pk_mul_f32 v[224:225], v[224:225], v[152:153]
	v_pk_mul_f32 v[226:227], v[226:227], v[154:155]
	v_pk_mul_f32 v[16:17], v[16:17], v[220:221]
	v_pk_mul_f32 v[18:19], v[18:19], v[222:223]
	v_pk_mul_f32 v[12:13], v[12:13], v[224:225]
	v_pk_mul_f32 v[14:15], v[14:15], v[226:227]
	s_waitcnt vmcnt(10)
	v_lshlrev_b32_e32 v220, 16, v156
	v_and_b32_e32 v221, 0xffff0000, v156
	v_lshlrev_b32_e32 v222, 16, v157
	v_and_b32_e32 v223, 0xffff0000, v157
	v_lshlrev_b32_e32 v224, 16, v158
	v_and_b32_e32 v225, 0xffff0000, v158
	v_lshlrev_b32_e32 v226, 16, v159
	v_and_b32_e32 v227, 0xffff0000, v159
	v_max_f32_e32 v220, 0x1e3ce508, v220
	v_max_f32_e32 v221, 0x1e3ce508, v221
	v_max_f32_e32 v222, 0x1e3ce508, v222
	v_max_f32_e32 v223, 0x1e3ce508, v223
	v_max_f32_e32 v224, 0x1e3ce508, v224
	v_max_f32_e32 v225, 0x1e3ce508, v225
	v_max_f32_e32 v226, 0x1e3ce508, v226
	v_max_f32_e32 v227, 0x1e3ce508, v227
	v_lshlrev_b32_e32 v156, 16, v160
	v_and_b32_e32 v157, 0xffff0000, v160
	v_lshlrev_b32_e32 v158, 16, v161
	v_and_b32_e32 v159, 0xffff0000, v161
	v_lshlrev_b32_e32 v160, 16, v162
	v_and_b32_e32 v161, 0xffff0000, v162
	v_lshlrev_b32_e32 v162, 16, v163
	v_and_b32_e32 v163, 0xffff0000, v163
	v_max_f32_e32 v156, 0x1e3ce508, v156
	v_max_f32_e32 v157, 0x1e3ce508, v157
	v_max_f32_e32 v158, 0x1e3ce508, v158
	v_max_f32_e32 v159, 0x1e3ce508, v159
	v_max_f32_e32 v160, 0x1e3ce508, v160
	v_max_f32_e32 v161, 0x1e3ce508, v161
	v_max_f32_e32 v162, 0x1e3ce508, v162
	v_max_f32_e32 v163, 0x1e3ce508, v163
	v_rcp_f32_e32 v156, v156
	v_rcp_f32_e32 v157, v157
	v_rcp_f32_e32 v158, v158
	v_rcp_f32_e32 v159, v159
	v_rcp_f32_e32 v160, v160
	v_rcp_f32_e32 v161, v161
	v_rcp_f32_e32 v162, v162
	v_rcp_f32_e32 v163, v163
	v_pk_mul_f32 v[220:221], v[220:221], v[156:157]
	v_pk_mul_f32 v[222:223], v[222:223], v[158:159]
	v_pk_mul_f32 v[224:225], v[224:225], v[160:161]
	v_pk_mul_f32 v[226:227], v[226:227], v[162:163]
	v_pk_mul_f32 v[40:41], v[40:41], v[220:221]
	v_pk_mul_f32 v[42:43], v[42:43], v[222:223]
	v_pk_mul_f32 v[36:37], v[36:37], v[224:225]
	v_pk_mul_f32 v[38:39], v[38:39], v[226:227]
	s_waitcnt vmcnt(8)
	v_lshlrev_b32_e32 v220, 16, v180
	v_and_b32_e32 v221, 0xffff0000, v180
	v_lshlrev_b32_e32 v222, 16, v181
	v_and_b32_e32 v223, 0xffff0000, v181
	v_lshlrev_b32_e32 v224, 16, v182
	v_and_b32_e32 v225, 0xffff0000, v182
	v_lshlrev_b32_e32 v226, 16, v183
	v_and_b32_e32 v227, 0xffff0000, v183
	v_max_f32_e32 v220, 0x1e3ce508, v220
	v_max_f32_e32 v221, 0x1e3ce508, v221
	v_max_f32_e32 v222, 0x1e3ce508, v222
	v_max_f32_e32 v223, 0x1e3ce508, v223
	v_max_f32_e32 v224, 0x1e3ce508, v224
	v_max_f32_e32 v225, 0x1e3ce508, v225
	v_max_f32_e32 v226, 0x1e3ce508, v226
	v_max_f32_e32 v227, 0x1e3ce508, v227
	v_lshlrev_b32_e32 v180, 16, v184
	v_and_b32_e32 v181, 0xffff0000, v184
	v_lshlrev_b32_e32 v182, 16, v185
	v_and_b32_e32 v183, 0xffff0000, v185
	v_lshlrev_b32_e32 v184, 16, v186
	v_and_b32_e32 v185, 0xffff0000, v186
	v_lshlrev_b32_e32 v186, 16, v187
	v_and_b32_e32 v187, 0xffff0000, v187
	v_max_f32_e32 v180, 0x1e3ce508, v180
	v_max_f32_e32 v181, 0x1e3ce508, v181
	v_max_f32_e32 v182, 0x1e3ce508, v182
	v_max_f32_e32 v183, 0x1e3ce508, v183
	v_max_f32_e32 v184, 0x1e3ce508, v184
	v_max_f32_e32 v185, 0x1e3ce508, v185
	v_max_f32_e32 v186, 0x1e3ce508, v186
	v_max_f32_e32 v187, 0x1e3ce508, v187
	v_rcp_f32_e32 v180, v180
	v_rcp_f32_e32 v181, v181
	v_rcp_f32_e32 v182, v182
	v_rcp_f32_e32 v183, v183
	v_rcp_f32_e32 v184, v184
	v_rcp_f32_e32 v185, v185
	v_rcp_f32_e32 v186, v186
	v_rcp_f32_e32 v187, v187
	v_pk_mul_f32 v[220:221], v[220:221], v[180:181]
	v_pk_mul_f32 v[222:223], v[222:223], v[182:183]
	v_pk_mul_f32 v[224:225], v[224:225], v[184:185]
	v_pk_mul_f32 v[226:227], v[226:227], v[186:187]
	v_pk_mul_f32 v[8:9], v[8:9], v[220:221]
	v_pk_mul_f32 v[10:11], v[10:11], v[222:223]
	v_pk_mul_f32 v[4:5], v[4:5], v[224:225]
	v_pk_mul_f32 v[6:7], v[6:7], v[226:227]
	s_waitcnt vmcnt(6)
	v_lshlrev_b32_e32 v220, 16, v192
	v_and_b32_e32 v221, 0xffff0000, v192
	v_lshlrev_b32_e32 v222, 16, v193
	v_and_b32_e32 v223, 0xffff0000, v193
	v_lshlrev_b32_e32 v224, 16, v194
	v_and_b32_e32 v225, 0xffff0000, v194
	v_lshlrev_b32_e32 v226, 16, v195
	v_and_b32_e32 v227, 0xffff0000, v195
	v_max_f32_e32 v220, 0x1e3ce508, v220
	v_max_f32_e32 v221, 0x1e3ce508, v221
	v_max_f32_e32 v222, 0x1e3ce508, v222
	v_max_f32_e32 v223, 0x1e3ce508, v223
	v_max_f32_e32 v224, 0x1e3ce508, v224
	v_max_f32_e32 v225, 0x1e3ce508, v225
	v_max_f32_e32 v226, 0x1e3ce508, v226
	v_max_f32_e32 v227, 0x1e3ce508, v227
	v_lshlrev_b32_e32 v192, 16, v196
	v_and_b32_e32 v193, 0xffff0000, v196
	v_lshlrev_b32_e32 v194, 16, v197
	v_and_b32_e32 v195, 0xffff0000, v197
	v_lshlrev_b32_e32 v196, 16, v198
	v_and_b32_e32 v197, 0xffff0000, v198
	v_lshlrev_b32_e32 v198, 16, v199
	v_and_b32_e32 v199, 0xffff0000, v199
	v_max_f32_e32 v192, 0x1e3ce508, v192
	v_max_f32_e32 v193, 0x1e3ce508, v193
	v_max_f32_e32 v194, 0x1e3ce508, v194
	v_max_f32_e32 v195, 0x1e3ce508, v195
	v_max_f32_e32 v196, 0x1e3ce508, v196
	v_max_f32_e32 v197, 0x1e3ce508, v197
	v_max_f32_e32 v198, 0x1e3ce508, v198
	v_max_f32_e32 v199, 0x1e3ce508, v199
	v_rcp_f32_e32 v192, v192
	v_rcp_f32_e32 v193, v193
	v_rcp_f32_e32 v194, v194
	v_rcp_f32_e32 v195, v195
	v_rcp_f32_e32 v196, v196
	v_rcp_f32_e32 v197, v197
	v_rcp_f32_e32 v198, v198
	v_rcp_f32_e32 v199, v199
	v_pk_mul_f32 v[220:221], v[220:221], v[192:193]
	v_pk_mul_f32 v[222:223], v[222:223], v[194:195]
	v_pk_mul_f32 v[224:225], v[224:225], v[196:197]
	v_pk_mul_f32 v[226:227], v[226:227], v[198:199]
	v_pk_mul_f32 v[32:33], v[32:33], v[220:221]
	v_pk_mul_f32 v[34:35], v[34:35], v[222:223]
	v_pk_mul_f32 v[28:29], v[28:29], v[224:225]
	v_pk_mul_f32 v[30:31], v[30:31], v[226:227]
	s_waitcnt vmcnt(4)
	v_lshlrev_b32_e32 v220, 16, v212
	v_and_b32_e32 v221, 0xffff0000, v212
	v_lshlrev_b32_e32 v222, 16, v213
	v_and_b32_e32 v223, 0xffff0000, v213
	v_lshlrev_b32_e32 v224, 16, v214
	v_and_b32_e32 v225, 0xffff0000, v214
	v_lshlrev_b32_e32 v226, 16, v215
	v_and_b32_e32 v227, 0xffff0000, v215
	v_max_f32_e32 v220, 0x1e3ce508, v220
	v_max_f32_e32 v221, 0x1e3ce508, v221
	v_max_f32_e32 v222, 0x1e3ce508, v222
	v_max_f32_e32 v223, 0x1e3ce508, v223
	v_max_f32_e32 v224, 0x1e3ce508, v224
	v_max_f32_e32 v225, 0x1e3ce508, v225
	v_max_f32_e32 v226, 0x1e3ce508, v226
	v_max_f32_e32 v227, 0x1e3ce508, v227
	v_lshlrev_b32_e32 v212, 16, v216
	v_and_b32_e32 v213, 0xffff0000, v216
	v_lshlrev_b32_e32 v214, 16, v217
	v_and_b32_e32 v215, 0xffff0000, v217
	v_lshlrev_b32_e32 v216, 16, v218
	v_and_b32_e32 v217, 0xffff0000, v218
	v_lshlrev_b32_e32 v218, 16, v219
	v_and_b32_e32 v219, 0xffff0000, v219
	v_max_f32_e32 v212, 0x1e3ce508, v212
	v_max_f32_e32 v213, 0x1e3ce508, v213
	v_max_f32_e32 v214, 0x1e3ce508, v214
	v_max_f32_e32 v215, 0x1e3ce508, v215
	v_max_f32_e32 v216, 0x1e3ce508, v216
	v_max_f32_e32 v217, 0x1e3ce508, v217
	v_max_f32_e32 v218, 0x1e3ce508, v218
	v_max_f32_e32 v219, 0x1e3ce508, v219
	v_rcp_f32_e32 v212, v212
	v_rcp_f32_e32 v213, v213
	v_rcp_f32_e32 v214, v214
	v_rcp_f32_e32 v215, v215
	v_rcp_f32_e32 v216, v216
	v_rcp_f32_e32 v217, v217
	v_rcp_f32_e32 v218, v218
	v_rcp_f32_e32 v219, v219
	v_pk_mul_f32 v[220:221], v[220:221], v[212:213]
	v_pk_mul_f32 v[222:223], v[222:223], v[214:215]
	v_pk_mul_f32 v[224:225], v[224:225], v[216:217]
	v_pk_mul_f32 v[226:227], v[226:227], v[218:219]
	v_pk_mul_f32 v[116:117], v[116:117], v[220:221]
	v_pk_mul_f32 v[118:119], v[118:119], v[222:223]
	v_pk_mul_f32 v[120:121], v[120:121], v[224:225]
	v_pk_mul_f32 v[122:123], v[122:123], v[226:227]
	s_waitcnt vmcnt(2)
	v_lshlrev_b32_e32 v220, 16, v132
	v_and_b32_e32 v221, 0xffff0000, v132
	v_lshlrev_b32_e32 v222, 16, v133
	v_and_b32_e32 v223, 0xffff0000, v133
	v_lshlrev_b32_e32 v224, 16, v134
	v_and_b32_e32 v225, 0xffff0000, v134
	v_lshlrev_b32_e32 v226, 16, v135
	v_and_b32_e32 v227, 0xffff0000, v135
	v_max_f32_e32 v220, 0x1e3ce508, v220
	v_max_f32_e32 v221, 0x1e3ce508, v221
	v_max_f32_e32 v222, 0x1e3ce508, v222
	v_max_f32_e32 v223, 0x1e3ce508, v223
	v_max_f32_e32 v224, 0x1e3ce508, v224
	v_max_f32_e32 v225, 0x1e3ce508, v225
	v_max_f32_e32 v226, 0x1e3ce508, v226
	v_max_f32_e32 v227, 0x1e3ce508, v227
	v_lshlrev_b32_e32 v132, 16, v136
	v_and_b32_e32 v133, 0xffff0000, v136
	v_lshlrev_b32_e32 v134, 16, v137
	v_and_b32_e32 v135, 0xffff0000, v137
	v_lshlrev_b32_e32 v136, 16, v138
	v_and_b32_e32 v137, 0xffff0000, v138
	v_lshlrev_b32_e32 v138, 16, v139
	v_and_b32_e32 v139, 0xffff0000, v139
	v_max_f32_e32 v132, 0x1e3ce508, v132
	v_max_f32_e32 v133, 0x1e3ce508, v133
	v_max_f32_e32 v134, 0x1e3ce508, v134
	v_max_f32_e32 v135, 0x1e3ce508, v135
	v_max_f32_e32 v136, 0x1e3ce508, v136
	v_max_f32_e32 v137, 0x1e3ce508, v137
	v_max_f32_e32 v138, 0x1e3ce508, v138
	v_max_f32_e32 v139, 0x1e3ce508, v139
	v_rcp_f32_e32 v132, v132
	v_rcp_f32_e32 v133, v133
	v_rcp_f32_e32 v134, v134
	v_rcp_f32_e32 v135, v135
	v_rcp_f32_e32 v136, v136
	v_rcp_f32_e32 v137, v137
	v_rcp_f32_e32 v138, v138
	v_rcp_f32_e32 v139, v139
	v_pk_mul_f32 v[220:221], v[220:221], v[132:133]
	v_pk_mul_f32 v[222:223], v[222:223], v[134:135]
	v_pk_mul_f32 v[224:225], v[224:225], v[136:137]
	v_pk_mul_f32 v[226:227], v[226:227], v[138:139]
	v_pk_mul_f32 v[24:25], v[24:25], v[220:221]
	v_pk_mul_f32 v[26:27], v[26:27], v[222:223]
	v_pk_mul_f32 v[20:21], v[20:21], v[224:225]
	v_pk_mul_f32 v[22:23], v[22:23], v[226:227]
	s_waitcnt vmcnt(0)
	v_lshlrev_b32_e32 v220, 16, v140
	v_and_b32_e32 v221, 0xffff0000, v140
	v_lshlrev_b32_e32 v222, 16, v141
	v_and_b32_e32 v223, 0xffff0000, v141
	v_lshlrev_b32_e32 v224, 16, v142
	v_and_b32_e32 v225, 0xffff0000, v142
	v_lshlrev_b32_e32 v226, 16, v143
	v_and_b32_e32 v227, 0xffff0000, v143
	v_max_f32_e32 v220, 0x1e3ce508, v220
	v_max_f32_e32 v221, 0x1e3ce508, v221
	v_max_f32_e32 v222, 0x1e3ce508, v222
	v_max_f32_e32 v223, 0x1e3ce508, v223
	v_max_f32_e32 v224, 0x1e3ce508, v224
	v_max_f32_e32 v225, 0x1e3ce508, v225
	v_max_f32_e32 v226, 0x1e3ce508, v226
	v_max_f32_e32 v227, 0x1e3ce508, v227
	v_lshlrev_b32_e32 v140, 16, v144
	v_and_b32_e32 v141, 0xffff0000, v144
	v_lshlrev_b32_e32 v142, 16, v145
	v_and_b32_e32 v143, 0xffff0000, v145
	v_lshlrev_b32_e32 v144, 16, v146
	v_and_b32_e32 v145, 0xffff0000, v146
	v_lshlrev_b32_e32 v146, 16, v147
	v_and_b32_e32 v147, 0xffff0000, v147
	v_max_f32_e32 v140, 0x1e3ce508, v140
	v_max_f32_e32 v141, 0x1e3ce508, v141
	v_max_f32_e32 v142, 0x1e3ce508, v142
	v_max_f32_e32 v143, 0x1e3ce508, v143
	v_max_f32_e32 v144, 0x1e3ce508, v144
	v_max_f32_e32 v145, 0x1e3ce508, v145
	v_max_f32_e32 v146, 0x1e3ce508, v146
	v_max_f32_e32 v147, 0x1e3ce508, v147
	v_rcp_f32_e32 v140, v140
	v_rcp_f32_e32 v141, v141
	v_rcp_f32_e32 v142, v142
	v_rcp_f32_e32 v143, v143
	v_rcp_f32_e32 v144, v144
	v_rcp_f32_e32 v145, v145
	v_rcp_f32_e32 v146, v146
	v_rcp_f32_e32 v147, v147
	v_pk_mul_f32 v[220:221], v[220:221], v[140:141]
	v_pk_mul_f32 v[222:223], v[222:223], v[142:143]
	v_pk_mul_f32 v[224:225], v[224:225], v[144:145]
	v_pk_mul_f32 v[226:227], v[226:227], v[146:147]
	v_pk_mul_f32 v[124:125], v[124:125], v[220:221]
	v_pk_mul_f32 v[126:127], v[126:127], v[222:223]
	v_pk_mul_f32 v[128:129], v[128:129], v[224:225]
	v_pk_mul_f32 v[130:131], v[130:131], v[226:227]
	s_branch .Lmg_done
